# speedup vs baseline: 1.0247x; 1.0072x over previous
.Lk2f_b2:
	s_waitcnt lgkmcnt(0)
	s_barrier
	v_and_b32_e32 v1, 63, v0
	v_lshlrev_b32_e32 v6, 3, v1
	ds_read_b64 v[14:15], v6 offset:18688
	s_cmp_eq_u32 s4, 7
	s_cbranch_scc1 .Lk2f_w7
	s_setprio 1
	v_lshrrev_b32_e32 v3, 2, v1
	s_mul_i32 s5, s4, 14
	v_add_u32_e32 v6, s5, v3
	v_cmp_gt_u32_e32 vcc, 14, v3
	v_mov_b32_e32 v7, 0x7f
	v_mov_b32_e32 v8, 0x62
	v_and_b32_e32 v9, 3, v1
	v_cndmask_b32_e32 v7, v7, v6, vcc
	v_cndmask_b32_e32 v8, v8, v6, vcc
	v_lshlrev_b32_e32 v7, 2, v7
	v_mul_u32_u24_e32 v2, 0x90, v8
	ds_read_b32 v3, v7 offset:18688
	ds_read_b128 v[4:7], v2 offset:19456
	v_lshlrev_b32_e32 v1, 4, v9
	s_mov_b32 s32, s8
	s_and_b32 s33, s9, 0xffff
	s_mov_b32 s34, 0xc35000
	s_mov_b32 s35, 0x20000
	v_and_b32_e32 v8, 15, v0
	v_add_u32_e32 v9, s5, v8
	s_mul_i32 s6, s3, 0x62
	v_add_u32_e32 v9, s6, v9
	v_cmp_gt_u32_e32 vcc, 14, v8
	s_mov_b32 s7, 0x186a0
	v_cmp_gt_u32_e64 s[38:39], s7, v9
	s_and_b64 vcc, vcc, s[38:39]
	s_mov_b64 s[40:41], vcc
	v_and_b32_e32 v8, 0x30, v0
	v_cndmask_b32_e32 v9, 0, v9, vcc
	v_lshl_or_b32 v8, v9, 7, v8
	buffer_load_dwordx4 v[56:59], v8, s[32:35], 0 offen
	buffer_load_dwordx4 v[60:63], v8, s[32:35], 0 offen offset:64
	v_mov_b32_e32 v40, 0
	v_mov_b32_e32 v41, 0
	v_mov_b32_e32 v42, 0
	v_mov_b32_e32 v43, 0
	v_mov_b32_e32 v44, 0
	v_mov_b32_e32 v45, 0
	v_mov_b32_e32 v46, 0
	v_mov_b32_e32 v47, 0
	v_mov_b32_e32 v48, 0
	v_mov_b32_e32 v49, 0
	v_mov_b32_e32 v50, 0
	v_mov_b32_e32 v51, 0
	v_mov_b32_e32 v52, 0
	v_mov_b32_e32 v53, 0
	v_mov_b32_e32 v54, 0
	v_mov_b32_e32 v55, 0
	s_mov_b32 s5, 0
	s_waitcnt lgkmcnt(0)
	v_max_u32_e32 v8, v14, v15
	v_cmp_lt_u32_e32 vcc, 32, v8
	s_cmp_lg_u64 vcc, 0
	s_cbranch_scc1 .Lk2f_fallback
	v_cmp_lt_i32_e32 vcc, 0, v3
	s_cmp_lg_u64 vcc, 0
	s_cbranch_scc0 .Lk2f_gdone
